# edge1 XCD-aware tile assignment with runs of 32 workgroups (was 16)
# baseline (speedup 1.0000x reference)
.LBB4_4:
	s_or_b64 exec, exec, s[6:7]
	s_and_b32 s86, s2, 7
	s_lshl_b32 s86, s86, 5
	s_bfe_u32 s87, s2, 0x50003
	s_or_b32 s86, s86, s87
	s_and_b32 s87, s2, 0xffffff00
	s_or_b32 s2, s86, s87
	v_lshl_or_b32 v64, s2, 2, v48
	v_min_i32_e32 v48, 0x61a7, v64
	v_lshl_or_b32 v54, v48, 5, v66
	v_ashrrev_i32_e32 v55, 31, v54
	v_lshl_add_u64 v[56:57], v[54:55], 4, s[8:9]
	v_max_i32_e32 v48, 1, v54
	v_mov_b32_e32 v49, 0
	v_lshl_add_u64 v[58:59], v[48:49], 4, s[8:9]
	global_load_dwordx4 v[48:51], v[56:57], off
	global_load_dword v80, v[56:57], off offset:24
	global_load_dword v55, v[58:59], off offset:-8
	s_load_dword s10, s[0:1], 0x48
	s_waitcnt vmcnt(13)
	ds_write_b128 v46, v[14:17] offset:12800
	s_waitcnt vmcnt(12)
	ds_write_b128 v46, v[22:25] offset:16896
	s_waitcnt vmcnt(10)
	ds_write_b128 v46, v[42:45] offset:20992
	s_waitcnt vmcnt(9)
	v_cvt_f16_f32_e32 v14, v34
	v_cvt_f16_f32_e32 v15, v37
	v_cvt_pk_f16_f32 v17, v35, v36
	s_waitcnt vmcnt(8)
	v_cvt_f16_f32_e32 v23, v41
	v_pack_b32_f16 v16, v14, v17
	v_alignbit_b32 v17, v15, v17, 16
	v_cvt_f16_f32_e32 v15, v38
	v_cvt_pk_f16_f32 v24, v39, v40
	v_lshlrev_b32_e32 v14, 3, v0
	v_alignbit_b32 v23, v23, v24, 16
	v_pack_b32_f16 v22, v15, v24
	s_waitcnt vmcnt(7)
	v_cvt_f16_f32_e32 v15, v18
	ds_write2st64_b64 v14, v[16:17], v[22:23] offset1:4
	v_cvt_pk_f16_f32 v17, v19, v20
	v_cvt_f16_f32_e32 v18, v21
	v_pack_b32_f16 v16, v15, v17
	s_waitcnt vmcnt(6)
	v_cvt_f16_f32_e32 v15, v26
	v_cvt_f16_f32_e32 v19, v29
	s_waitcnt vmcnt(5)
	v_cvt_f16_f32_e32 v6, v6
	v_cvt_pk_f16_f32 v7, v7, v8
	v_cvt_f16_f32_e32 v8, v9
	s_waitcnt vmcnt(4)
	v_cvt_f16_f32_e32 v9, v10
	v_cvt_f16_f32_e32 v10, v13
	v_cvt_pk_f16_f32 v20, v27, v28
	v_cvt_pk_f16_f32 v11, v11, v12
	v_alignbit_b32 v17, v18, v17, 16
	v_pack_b32_f16 v18, v15, v20
	v_alignbit_b32 v19, v19, v20, 16
	v_pack_b32_f16 v6, v6, v7
	v_alignbit_b32 v7, v8, v7, 16
	v_pack_b32_f16 v8, v9, v11
	v_alignbit_b32 v9, v10, v11, 16
	ds_write_b128 v46, v[30:33] offset:25088
	ds_write2st64_b64 v14, v[16:17], v[18:19] offset0:8 offset1:12
	ds_write2st64_b64 v14, v[6:7], v[8:9] offset0:16 offset1:20
	s_and_saveexec_b64 s[2:3], vcc
	s_cbranch_execnz .LBB4_74
	s_or_b64 exec, exec, s[2:3]
	s_and_saveexec_b64 s[2:3], vcc
	s_cbranch_execnz .LBB4_75
